# grid barrier: the 17th arriver of each XCD issues one early L2 write-back so the XCD leader's release-time write-back has less dirty data
# speedup vs baseline: 1.0088x; 1.0088x over previous
.LBB0_265:
	v_readlane_b32 s4, v254, 37
	s_lshl_b32 s4, s4, 2
	s_add_u32 s25, s2, s4
	s_addc_u32 s24, s3, 0
	v_mov_b32_e32 v1, s25
	v_add_co_u32_e32 v4, vcc, 0x1000, v1
	v_mov_b32_e32 v1, s24
	s_nop 0
	v_addc_co_u32_e32 v5, vcc, 0, v1, vcc
	flat_atomic_add v3, v[4:5], v193 offset:1024 sc0
	v_cvt_f32_u32_e32 v1, v2
	v_sub_u32_e32 v4, 0, v2
	v_rcp_iflag_f32_e32 v1, v1
	s_nop 0
	v_mul_f32_e32 v1, 0x4f7ffffe, v1
	v_cvt_u32_f32_e32 v1, v1
	v_mul_lo_u32 v4, v4, v1
	v_mul_hi_u32 v4, v1, v4
	v_add_u32_e32 v1, v1, v4
	s_waitcnt vmcnt(0) lgkmcnt(0)
	v_and_b32_e32 v5, 31, v3
	v_cmp_eq_u32_e32 vcc, 16, v5
	s_nop 4
	s_cbranch_vccz .Lhalf_flush_11
	buffer_wbl2 sc1
.Lhalf_flush_11:
	v_mul_hi_u32 v1, v3, v1
	v_mul_lo_u32 v4, v1, v2
	v_sub_u32_e32 v4, v3, v4
	v_cmp_ge_u32_e32 vcc, v4, v2
	v_add_u32_e32 v5, 1, v1
	s_nop 0
	v_cndmask_b32_e32 v1, v1, v5, vcc
	v_sub_u32_e32 v5, v4, v2
	v_cndmask_b32_e32 v4, v4, v5, vcc
	v_cmp_ge_u32_e32 vcc, v4, v2
	v_add_u32_e32 v4, 1, v1
	s_nop 0
	v_cndmask_b32_e32 v1, v1, v4, vcc
	v_add_u32_e32 v4, 1, v3
	v_mad_u64_u32 v[2:3], s[4:5], v2, v1, v[2:3]
	v_cmp_ne_u32_e32 vcc, v4, v2
	s_and_saveexec_b64 s[4:5], vcc
	s_xor_b64 s[4:5], exec, s[4:5]
	s_cbranch_execz .LBB0_278
	v_mov_b32_e32 v0, s25
	v_add_co_u32_e32 v2, vcc, 0x2000, v0
	v_mov_b32_e32 v0, s24
	s_nop 0
	v_addc_co_u32_e32 v3, vcc, 0, v0, vcc
	flat_load_dword v0, v[2:3] offset:1024 sc1
	s_add_u32 s8, s25, 0x2400
	s_addc_u32 s9, s24, 0
	s_waitcnt vmcnt(0) lgkmcnt(0)
	v_cmp_eq_u32_e32 vcc, v0, v1
	s_and_saveexec_b64 s[6:7], vcc
	s_cbranch_execz .LBB0_277
	s_mov_b32 s26, 1
	s_mov_b64 s[10:11], 0
	s_branch .LBB0_269

.LBB0_353:
	v_readlane_b32 s4, v254, 37
	s_lshl_b32 s4, s4, 2
	s_add_u32 s27, s2, s4
	s_addc_u32 s26, s3, 0
	v_mov_b32_e32 v1, s27
	v_add_co_u32_e32 v4, vcc, 0x1000, v1
	v_mov_b32_e32 v1, s26
	s_nop 0
	v_addc_co_u32_e32 v5, vcc, 0, v1, vcc
	flat_atomic_add v3, v[4:5], v193 offset:1024 sc0
	v_cvt_f32_u32_e32 v1, v2
	v_sub_u32_e32 v4, 0, v2
	v_rcp_iflag_f32_e32 v1, v1
	s_nop 0
	v_mul_f32_e32 v1, 0x4f7ffffe, v1
	v_cvt_u32_f32_e32 v1, v1
	v_mul_lo_u32 v4, v4, v1
	v_mul_hi_u32 v4, v1, v4
	v_add_u32_e32 v1, v1, v4
	s_waitcnt vmcnt(0) lgkmcnt(0)
	v_and_b32_e32 v5, 31, v3
	v_cmp_eq_u32_e32 vcc, 16, v5
	s_nop 4
	s_cbranch_vccz .Lhalf_flush_10
	buffer_wbl2 sc1
.Lhalf_flush_10:
	v_mul_hi_u32 v1, v3, v1
	v_mul_lo_u32 v4, v1, v2
	v_sub_u32_e32 v4, v3, v4
	v_cmp_ge_u32_e32 vcc, v4, v2
	v_add_u32_e32 v5, 1, v1
	s_nop 0
	v_cndmask_b32_e32 v1, v1, v5, vcc
	v_sub_u32_e32 v5, v4, v2
	v_cndmask_b32_e32 v4, v4, v5, vcc
	v_cmp_ge_u32_e32 vcc, v4, v2
	v_add_u32_e32 v4, 1, v1
	s_nop 0
	v_cndmask_b32_e32 v1, v1, v4, vcc
	v_add_u32_e32 v4, 1, v3
	v_mad_u64_u32 v[2:3], s[4:5], v2, v1, v[2:3]
	v_cmp_ne_u32_e32 vcc, v4, v2
	s_and_saveexec_b64 s[4:5], vcc
	s_xor_b64 s[4:5], exec, s[4:5]
	s_cbranch_execz .LBB0_366
	v_mov_b32_e32 v0, s27
	v_add_co_u32_e32 v2, vcc, 0x2000, v0
	v_mov_b32_e32 v0, s26
	s_nop 0
	v_addc_co_u32_e32 v3, vcc, 0, v0, vcc
	flat_load_dword v0, v[2:3] offset:1024 sc1
	s_add_u32 s8, s27, 0x2400
	s_addc_u32 s9, s26, 0
	s_waitcnt vmcnt(0) lgkmcnt(0)
	v_cmp_eq_u32_e32 vcc, v0, v1
	s_and_saveexec_b64 s[6:7], vcc
	s_cbranch_execz .LBB0_365
	s_mov_b32 s30, 1
	s_mov_b64 s[12:13], 0
	s_branch .LBB0_357

.LBB0_583:
	v_readlane_b32 s6, v254, 37
	s_lshl_b32 s6, s6, 2
	s_add_u32 s30, s2, s6
	s_addc_u32 s29, s3, 0
	v_mov_b32_e32 v1, s30
	v_add_co_u32_e32 v4, vcc, 0x1000, v1
	v_mov_b32_e32 v1, s29
	s_nop 0
	v_addc_co_u32_e32 v5, vcc, 0, v1, vcc
	flat_atomic_add v3, v[4:5], v193 offset:1024 sc0
	v_cvt_f32_u32_e32 v1, v2
	v_sub_u32_e32 v4, 0, v2
	v_rcp_iflag_f32_e32 v1, v1
	s_nop 0
	v_mul_f32_e32 v1, 0x4f7ffffe, v1
	v_cvt_u32_f32_e32 v1, v1
	v_mul_lo_u32 v4, v4, v1
	v_mul_hi_u32 v4, v1, v4
	v_add_u32_e32 v1, v1, v4
	s_waitcnt vmcnt(0) lgkmcnt(0)
	v_and_b32_e32 v5, 31, v3
	v_cmp_eq_u32_e32 vcc, 16, v5
	s_nop 4
	s_cbranch_vccz .Lhalf_flush_7
	buffer_wbl2 sc1
.Lhalf_flush_7:
	v_mul_hi_u32 v1, v3, v1
	v_mul_lo_u32 v4, v1, v2
	v_sub_u32_e32 v4, v3, v4
	v_cmp_ge_u32_e32 vcc, v4, v2
	v_add_u32_e32 v5, 1, v1
	s_nop 0
	v_cndmask_b32_e32 v1, v1, v5, vcc
	v_sub_u32_e32 v5, v4, v2
	v_cndmask_b32_e32 v4, v4, v5, vcc
	v_cmp_ge_u32_e32 vcc, v4, v2
	v_add_u32_e32 v4, 1, v1
	s_nop 0
	v_cndmask_b32_e32 v1, v1, v4, vcc
	v_add_u32_e32 v4, 1, v3
	v_mad_u64_u32 v[2:3], s[6:7], v2, v1, v[2:3]
	v_cmp_ne_u32_e32 vcc, v4, v2
	s_and_saveexec_b64 s[6:7], vcc
	s_xor_b64 s[6:7], exec, s[6:7]
	s_cbranch_execz .LBB0_596
	v_mov_b32_e32 v0, s30
	v_add_co_u32_e32 v2, vcc, 0x2000, v0
	v_mov_b32_e32 v0, s29
	s_nop 0
	v_addc_co_u32_e32 v3, vcc, 0, v0, vcc
	flat_load_dword v0, v[2:3] offset:1024 sc1
	s_add_u32 s12, s30, 0x2400
	s_addc_u32 s13, s29, 0
	s_waitcnt vmcnt(0) lgkmcnt(0)
	v_cmp_eq_u32_e32 vcc, v0, v1
	s_and_saveexec_b64 s[8:9], vcc
	s_cbranch_execz .LBB0_595
	s_mov_b32 s33, 1
	s_mov_b64 s[14:15], 0
	s_branch .LBB0_587

.LBB0_689:
	v_readlane_b32 s4, v254, 37
	s_lshl_b32 s4, s4, 2
	s_add_u32 s9, s2, s4
	s_addc_u32 s8, s3, 0
	v_mov_b32_e32 v1, s9
	v_add_co_u32_e32 v4, vcc, 0x1000, v1
	v_mov_b32_e32 v1, s8
	s_nop 0
	v_addc_co_u32_e32 v5, vcc, 0, v1, vcc
	flat_atomic_add v3, v[4:5], v193 offset:1024 sc0
	v_cvt_f32_u32_e32 v1, v2
	v_sub_u32_e32 v4, 0, v2
	v_rcp_iflag_f32_e32 v1, v1
	s_nop 0
	v_mul_f32_e32 v1, 0x4f7ffffe, v1
	v_cvt_u32_f32_e32 v1, v1
	v_mul_lo_u32 v4, v4, v1
	v_mul_hi_u32 v4, v1, v4
	v_add_u32_e32 v1, v1, v4
	s_waitcnt vmcnt(0) lgkmcnt(0)
	v_and_b32_e32 v5, 31, v3
	v_cmp_eq_u32_e32 vcc, 16, v5
	s_nop 4
	s_cbranch_vccz .Lhalf_flush_6
	buffer_wbl2 sc1
.Lhalf_flush_6:
	v_mul_hi_u32 v1, v3, v1
	v_mul_lo_u32 v4, v1, v2
	v_sub_u32_e32 v4, v3, v4
	v_cmp_ge_u32_e32 vcc, v4, v2
	v_add_u32_e32 v5, 1, v1
	s_nop 0
	v_cndmask_b32_e32 v1, v1, v5, vcc
	v_sub_u32_e32 v5, v4, v2
	v_cndmask_b32_e32 v4, v4, v5, vcc
	v_cmp_ge_u32_e32 vcc, v4, v2
	v_add_u32_e32 v4, 1, v1
	s_nop 0
	v_cndmask_b32_e32 v1, v1, v4, vcc
	v_add_u32_e32 v4, 1, v3
	v_mad_u64_u32 v[2:3], s[4:5], v2, v1, v[2:3]
	v_cmp_ne_u32_e32 vcc, v4, v2
	s_and_saveexec_b64 s[4:5], vcc
	s_xor_b64 s[4:5], exec, s[4:5]
	s_cbranch_execz .LBB0_702
	v_mov_b32_e32 v0, s9
	v_add_co_u32_e32 v2, vcc, 0x2000, v0
	v_mov_b32_e32 v0, s8
	s_nop 0
	v_addc_co_u32_e32 v3, vcc, 0, v0, vcc
	flat_load_dword v0, v[2:3] offset:1024 sc1
	s_add_u32 s10, s9, 0x2400
	s_addc_u32 s11, s8, 0
	s_waitcnt vmcnt(0) lgkmcnt(0)
	v_cmp_eq_u32_e32 vcc, v0, v1
	s_and_saveexec_b64 s[6:7], vcc
	s_cbranch_execz .LBB0_701
	s_mov_b32 s26, 1
	s_mov_b64 s[12:13], 0
	s_branch .LBB0_693
